# poll cadence: s_sleep removed from the grid-barrier and row-tile hand-off poll loops (back-to-back polls)
# baseline (speedup 1.0000x reference)
; __device__ __forceinline__ unsigned xb_ld(unsigned* p)              { return __hip_atomic_load(p, __ATOMIC_RELAXED, __HIP_MEMORY_SCOPE_AGENT); }
; #define XB_SPIN(cond, bar) do { unsigned _sp = 0; while (cond) { __builtin_amdgcn_s_sleep(1); \
;     if ((++_sp & 255u) == 0u) { if (xb_ld(&(bar)[XB_TMO])) break; if (_sp > XB_SPIN_CAP) { atomicAdd(&(bar)[XB_TMO], 1u); break; } } } } while (0)
; __device__ __forceinline__ void xcd_barrier(const XcdBarrier& b) {
;     ...
;       else XB_SPIN(xb_ld(&bar[XB_TOPGEN]) == tg, bar);
.Lgb_w_1:
	global_load_dword v254, v253, s[44:45] offset:64 sc1
	s_waitcnt vmcnt(0)
	v_cmp_le_u32_e32 vcc, s99, v254
	s_cbranch_vccnz .Lgb_wd_1
	s_add_u32 s100, s100, 1
	s_cmp_lt_u32 s100, 0x1000
	s_cbranch_scc1 .Lgb_w_1

; __device__ __forceinline__ unsigned xb_ld(unsigned* p)              { return __hip_atomic_load(p, __ATOMIC_RELAXED, __HIP_MEMORY_SCOPE_AGENT); }
; #define XB_SPIN(cond, bar) do { unsigned _sp = 0; while (cond) { __builtin_amdgcn_s_sleep(1); \
;     if ((++_sp & 255u) == 0u) { if (xb_ld(&(bar)[XB_TMO])) break; if (_sp > XB_SPIN_CAP) { atomicAdd(&(bar)[XB_TMO], 1u); break; } } } } while (0)
; __device__ __forceinline__ void xcd_barrier(const XcdBarrier& b) {
;     ...
;       XB_SPIN(xb_ld(&bar[XB_XGEN(b.x)]) == gen, bar);
.Lmy_gs_w_8:
	global_load_dword v254, v253, s[44:45] offset:128 sc1
	s_waitcnt vmcnt(0)
	v_cmp_le_u32_e32 vcc, 8, v254
	s_cbranch_vccnz .Lgb_wd_8
	s_add_u32 s100, s100, 1
	s_cmp_lt_u32 s100, 0x100000
	s_cbranch_scc1 .Lmy_gs_w_8
	s_branch .Lgb_wd_8

; __device__ __forceinline__ unsigned xb_ld(unsigned* p)              { return __hip_atomic_load(p, __ATOMIC_RELAXED, __HIP_MEMORY_SCOPE_AGENT); }
; #define XB_SPIN(cond, bar) do { unsigned _sp = 0; while (cond) { __builtin_amdgcn_s_sleep(1); \
;     if ((++_sp & 255u) == 0u) { if (xb_ld(&(bar)[XB_TMO])) break; if (_sp > XB_SPIN_CAP) { atomicAdd(&(bar)[XB_TMO], 1u); break; } } } } while (0)
; __device__ __forceinline__ void xcd_barrier(const XcdBarrier& b) {
;     ...
;       XB_SPIN(xb_ld(&bar[XB_XGEN(b.x)]) == gen, bar);
.Lmy_gs_w_9:
	global_load_dword v254, v253, s[44:45] offset:128 sc1
	s_waitcnt vmcnt(0)
	v_cmp_le_u32_e32 vcc, 16, v254
	s_cbranch_vccnz .Lgb_wd_9
	s_add_u32 s100, s100, 1
	s_cmp_lt_u32 s100, 0x100000
	s_cbranch_scc1 .Lmy_gs_w_9
	s_branch .Lgb_wd_9
